# also drop the 12 compiler-duplicated lgkmcnt(0) waits in the GEMM K loops
# speedup vs baseline: 1.0171x; 1.0015x over previous
.LBB2_21:
	ds_read_b128 v[150:153], v145
	ds_read_b128 v[154:157], v145 offset:1024
	ds_read_b128 v[158:161], v145 offset:2048
	ds_read_b128 v[162:165], v145 offset:3072
	s_add_i32 s65, s28, 2
	s_add_u32 s30, s26, 0x80
	s_addc_u32 s29, s27, 0
	s_cmp_eq_u32 s55, s28
	s_cselect_b32 s28, s4, s30
	s_cselect_b32 s29, s5, s29
	s_cselect_b32 s31, s7, s64
	s_cselect_b32 s30, s6, s63
	v_lshl_add_u64 v[142:143], s[26:27], 0, v[136:137]
	s_add_i32 m0, s43, 0xc000
	ds_read_b128 v[166:169], v146
	ds_read_b128 v[170:173], v146 offset:1024
	ds_read_b128 v[174:177], v146 offset:2048
	ds_read_b128 v[178:181], v146 offset:3072
	ds_read_b128 v[182:185], v146 offset:4096
	ds_read_b128 v[186:189], v146 offset:5120
	ds_read_b128 v[190:193], v146 offset:6144
	ds_read_b128 v[194:197], v146 offset:7168
	global_load_lds_dwordx4 v[142:143], off
	v_lshl_add_u64 v[142:143], s[26:27], 0, v[134:135]
	s_add_i32 m0, s43, 0xe000
	s_nop 0
	global_load_lds_dwordx4 v[142:143], off
	s_waitcnt lgkmcnt(8)
	s_barrier
	s_waitcnt lgkmcnt(0)
	v_mfma_f32_16x16x32_f16 v[126:129], v[150:153], v[166:169], v[126:129]
	v_mfma_f32_16x16x32_f16 v[122:125], v[158:161], v[166:169], v[122:125]
	v_mfma_f32_16x16x32_f16 v[110:113], v[150:153], v[174:177], v[110:113]
	v_mfma_f32_16x16x32_f16 v[106:109], v[158:161], v[174:177], v[106:109]
	v_mfma_f32_16x16x32_f16 v[94:97], v[150:153], v[182:185], v[94:97]
	v_mfma_f32_16x16x32_f16 v[90:93], v[158:161], v[182:185], v[90:93]
	v_mfma_f32_16x16x32_f16 v[78:81], v[150:153], v[190:193], v[78:81]
	v_mfma_f32_16x16x32_f16 v[74:77], v[158:161], v[190:193], v[74:77]
	v_mfma_f32_16x16x32_f16 v[126:129], v[154:157], v[170:173], v[126:129]
	v_mfma_f32_16x16x32_f16 v[122:125], v[162:165], v[170:173], v[122:125]
	v_mfma_f32_16x16x32_f16 v[110:113], v[154:157], v[178:181], v[110:113]
	v_mfma_f32_16x16x32_f16 v[106:109], v[162:165], v[178:181], v[106:109]
	v_mfma_f32_16x16x32_f16 v[94:97], v[154:157], v[186:189], v[94:97]
	v_mfma_f32_16x16x32_f16 v[90:93], v[162:165], v[186:189], v[90:93]
	v_mfma_f32_16x16x32_f16 v[78:81], v[154:157], v[194:197], v[78:81]
	v_mfma_f32_16x16x32_f16 v[74:77], v[162:165], v[194:197], v[74:77]
	s_barrier
	s_add_i32 s66, s57, s40
	v_lshl_add_u64 v[142:143], s[30:31], 0, v[130:131]
	s_mov_b32 m0, s66
	ds_read_b128 v[198:201], v147
	ds_read_b128 v[202:205], v147 offset:1024
	ds_read_b128 v[206:209], v147 offset:2048
	ds_read_b128 v[210:213], v147 offset:3072
	global_load_lds_dwordx4 v[142:143], off
	v_lshl_add_u64 v[214:215], s[30:31], 0, v[132:133]
	s_add_i32 m0, s66, 0x2000
	s_nop 0
	global_load_lds_dwordx4 v[214:215], off
	s_barrier
	s_waitcnt lgkmcnt(0)
	v_mfma_f32_16x16x32_f16 v[118:121], v[198:201], v[166:169], v[118:121]
	v_mfma_f32_16x16x32_f16 v[114:117], v[206:209], v[166:169], v[114:117]
	v_mfma_f32_16x16x32_f16 v[102:105], v[198:201], v[174:177], v[102:105]
	v_mfma_f32_16x16x32_f16 v[98:101], v[206:209], v[174:177], v[98:101]
	v_mfma_f32_16x16x32_f16 v[86:89], v[198:201], v[182:185], v[86:89]
	v_mfma_f32_16x16x32_f16 v[82:85], v[206:209], v[182:185], v[82:85]
	v_mfma_f32_16x16x32_f16 v[70:73], v[198:201], v[190:193], v[70:73]
	v_mfma_f32_16x16x32_f16 v[66:69], v[206:209], v[190:193], v[66:69]
	v_mfma_f32_16x16x32_f16 v[118:121], v[202:205], v[170:173], v[118:121]
	v_mfma_f32_16x16x32_f16 v[114:117], v[210:213], v[170:173], v[114:117]
	v_mfma_f32_16x16x32_f16 v[102:105], v[202:205], v[178:181], v[102:105]
	v_mfma_f32_16x16x32_f16 v[98:101], v[210:213], v[178:181], v[98:101]
	v_mfma_f32_16x16x32_f16 v[86:89], v[202:205], v[186:189], v[86:89]
	v_mfma_f32_16x16x32_f16 v[82:85], v[210:213], v[186:189], v[82:85]
	v_mfma_f32_16x16x32_f16 v[70:73], v[202:205], v[194:197], v[70:73]
	v_mfma_f32_16x16x32_f16 v[66:69], v[210:213], v[194:197], v[66:69]
	s_mov_b32 m0, s43
	v_lshl_add_u64 v[216:217], s[28:29], 0, v[130:131]
	s_barrier
	ds_read_b128 v[166:169], v146 offset:16384
	ds_read_b128 v[170:173], v146 offset:17408
	ds_read_b128 v[174:177], v146 offset:18432
	ds_read_b128 v[178:181], v146 offset:19456
	ds_read_b128 v[182:185], v146 offset:20480
	ds_read_b128 v[186:189], v146 offset:21504
	ds_read_b128 v[190:193], v146 offset:22528
	ds_read_b128 v[194:197], v146 offset:23552
	global_load_lds_dwordx4 v[216:217], off
	v_lshl_add_u64 v[218:219], s[28:29], 0, v[132:133]
	s_mov_b32 m0, s44
	s_nop 0
	global_load_lds_dwordx4 v[218:219], off
	s_barrier
	s_waitcnt lgkmcnt(0)
	v_mfma_f32_16x16x32_f16 v[62:65], v[150:153], v[166:169], v[62:65]
	v_mfma_f32_16x16x32_f16 v[58:61], v[158:161], v[166:169], v[58:61]
	v_mfma_f32_16x16x32_f16 v[46:49], v[150:153], v[174:177], v[46:49]
	v_mfma_f32_16x16x32_f16 v[42:45], v[158:161], v[174:177], v[42:45]
	v_mfma_f32_16x16x32_f16 v[30:33], v[150:153], v[182:185], v[30:33]
	v_mfma_f32_16x16x32_f16 v[26:29], v[158:161], v[182:185], v[26:29]
	v_mfma_f32_16x16x32_f16 v[14:17], v[150:153], v[190:193], v[14:17]
	v_mfma_f32_16x16x32_f16 v[10:13], v[158:161], v[190:193], v[10:13]
	v_mfma_f32_16x16x32_f16 v[62:65], v[154:157], v[170:173], v[62:65]
	v_mfma_f32_16x16x32_f16 v[58:61], v[162:165], v[170:173], v[58:61]
	v_mfma_f32_16x16x32_f16 v[46:49], v[154:157], v[178:181], v[46:49]
	v_mfma_f32_16x16x32_f16 v[42:45], v[162:165], v[178:181], v[42:45]
	v_mfma_f32_16x16x32_f16 v[30:33], v[154:157], v[186:189], v[30:33]
	v_mfma_f32_16x16x32_f16 v[26:29], v[162:165], v[186:189], v[26:29]
	v_mfma_f32_16x16x32_f16 v[14:17], v[154:157], v[194:197], v[14:17]
	v_mfma_f32_16x16x32_f16 v[10:13], v[162:165], v[194:197], v[10:13]
	s_barrier
	s_add_u32 s30, s30, s10
	s_addc_u32 s31, s31, s11
	s_add_i32 s66, s58, s40
	v_lshl_add_u64 v[220:221], s[30:31], 0, v[130:131]
	s_mov_b32 m0, s66
	v_lshl_add_u64 v[222:223], s[30:31], 0, v[132:133]
	global_load_lds_dwordx4 v[220:221], off
	s_add_i32 m0, s66, 0x2000
	s_nop 0
	global_load_lds_dwordx4 v[222:223], off
	s_waitcnt vmcnt(6)
	s_barrier
	v_mfma_f32_16x16x32_f16 v[54:57], v[198:201], v[166:169], v[54:57]
	v_mfma_f32_16x16x32_f16 v[50:53], v[206:209], v[166:169], v[50:53]
	v_mfma_f32_16x16x32_f16 v[38:41], v[198:201], v[174:177], v[38:41]
	v_mfma_f32_16x16x32_f16 v[34:37], v[206:209], v[174:177], v[34:37]
	v_mfma_f32_16x16x32_f16 v[22:25], v[198:201], v[182:185], v[22:25]
	v_mfma_f32_16x16x32_f16 v[18:21], v[206:209], v[182:185], v[18:21]
	v_mfma_f32_16x16x32_f16 v[6:9], v[198:201], v[190:193], v[6:9]
	v_mfma_f32_16x16x32_f16 v[2:5], v[206:209], v[190:193], v[2:5]
	v_mfma_f32_16x16x32_f16 v[54:57], v[202:205], v[170:173], v[54:57]
	v_mfma_f32_16x16x32_f16 v[50:53], v[210:213], v[170:173], v[50:53]
	v_mfma_f32_16x16x32_f16 v[38:41], v[202:205], v[178:181], v[38:41]
	v_mfma_f32_16x16x32_f16 v[34:37], v[210:213], v[178:181], v[34:37]
	v_mfma_f32_16x16x32_f16 v[22:25], v[202:205], v[186:189], v[22:25]
	v_mfma_f32_16x16x32_f16 v[18:21], v[210:213], v[186:189], v[18:21]
	v_mfma_f32_16x16x32_f16 v[6:9], v[202:205], v[194:197], v[6:9]
	v_mfma_f32_16x16x32_f16 v[2:5], v[210:213], v[194:197], v[2:5]
	s_add_i32 s30, 0, 0x18000
	v_add_u32_e32 v140, s30, v141
	s_barrier
	ds_read_b128 v[150:153], v140
	ds_read_b128 v[154:157], v140 offset:1024
	ds_read_b128 v[158:161], v140 offset:2048
	ds_read_b128 v[162:165], v140 offset:3072
	s_add_u32 s28, s28, s10
	s_addc_u32 s29, s29, s11
	s_mov_b32 m0, s45
	v_lshl_add_u64 v[198:199], s[28:29], 0, v[130:131]
	ds_read_b128 v[166:169], v146 offset:32768
	ds_read_b128 v[170:173], v146 offset:33792
	ds_read_b128 v[174:177], v146 offset:34816
	ds_read_b128 v[178:181], v146 offset:35840
	ds_read_b128 v[182:185], v146 offset:36864
	ds_read_b128 v[186:189], v146 offset:37888
	ds_read_b128 v[190:193], v146 offset:38912
	ds_read_b128 v[194:197], v146 offset:39936
	global_load_lds_dwordx4 v[198:199], off
	v_lshl_add_u64 v[198:199], s[28:29], 0, v[132:133]
	s_mov_b32 m0, s46
	s_nop 0
	global_load_lds_dwordx4 v[198:199], off
	s_waitcnt lgkmcnt(8)
	s_barrier
	s_waitcnt lgkmcnt(0)
	v_mfma_f32_16x16x32_f16 v[126:129], v[150:153], v[166:169], v[126:129]
	v_mfma_f32_16x16x32_f16 v[122:125], v[158:161], v[166:169], v[122:125]
	v_mfma_f32_16x16x32_f16 v[110:113], v[150:153], v[174:177], v[110:113]
	v_mfma_f32_16x16x32_f16 v[106:109], v[158:161], v[174:177], v[106:109]
	v_mfma_f32_16x16x32_f16 v[94:97], v[150:153], v[182:185], v[94:97]
	v_mfma_f32_16x16x32_f16 v[90:93], v[158:161], v[182:185], v[90:93]
	v_mfma_f32_16x16x32_f16 v[78:81], v[150:153], v[190:193], v[78:81]
	v_mfma_f32_16x16x32_f16 v[74:77], v[158:161], v[190:193], v[74:77]
	v_mfma_f32_16x16x32_f16 v[126:129], v[154:157], v[170:173], v[126:129]
	v_mfma_f32_16x16x32_f16 v[122:125], v[162:165], v[170:173], v[122:125]
	v_mfma_f32_16x16x32_f16 v[110:113], v[154:157], v[178:181], v[110:113]
	v_mfma_f32_16x16x32_f16 v[106:109], v[162:165], v[178:181], v[106:109]
	v_mfma_f32_16x16x32_f16 v[94:97], v[154:157], v[186:189], v[94:97]
	v_mfma_f32_16x16x32_f16 v[90:93], v[162:165], v[186:189], v[90:93]
	v_mfma_f32_16x16x32_f16 v[78:81], v[154:157], v[194:197], v[78:81]
	v_mfma_f32_16x16x32_f16 v[74:77], v[162:165], v[194:197], v[74:77]
	s_barrier
	s_add_i32 s28, 0, 0x1c000
	s_add_i32 s29, s30, s40
	v_add_u32_e32 v140, s28, v141
	v_lshl_add_u64 v[142:143], v[142:143], 0, s[22:23]
	s_mov_b32 m0, s29
	ds_read_b128 v[198:201], v140
	ds_read_b128 v[202:205], v140 offset:1024
	ds_read_b128 v[206:209], v140 offset:2048
	ds_read_b128 v[210:213], v140 offset:3072
	global_load_lds_dwordx4 v[142:143], off
	v_lshl_add_u64 v[142:143], v[214:215], 0, s[22:23]
	s_add_i32 m0, s29, 0x2000
	s_nop 0
	global_load_lds_dwordx4 v[142:143], off
	s_barrier
	s_waitcnt lgkmcnt(0)
	v_mfma_f32_16x16x32_f16 v[118:121], v[198:201], v[166:169], v[118:121]
	v_mfma_f32_16x16x32_f16 v[114:117], v[206:209], v[166:169], v[114:117]
	v_mfma_f32_16x16x32_f16 v[102:105], v[198:201], v[174:177], v[102:105]
	v_mfma_f32_16x16x32_f16 v[98:101], v[206:209], v[174:177], v[98:101]
	v_mfma_f32_16x16x32_f16 v[86:89], v[198:201], v[182:185], v[86:89]
	v_mfma_f32_16x16x32_f16 v[82:85], v[206:209], v[182:185], v[82:85]
	v_mfma_f32_16x16x32_f16 v[70:73], v[198:201], v[190:193], v[70:73]
	v_mfma_f32_16x16x32_f16 v[66:69], v[206:209], v[190:193], v[66:69]
	v_mfma_f32_16x16x32_f16 v[118:121], v[202:205], v[170:173], v[118:121]
	v_mfma_f32_16x16x32_f16 v[114:117], v[210:213], v[170:173], v[114:117]
	v_mfma_f32_16x16x32_f16 v[102:105], v[202:205], v[178:181], v[102:105]
	v_mfma_f32_16x16x32_f16 v[98:101], v[210:213], v[178:181], v[98:101]
	v_mfma_f32_16x16x32_f16 v[86:89], v[202:205], v[186:189], v[86:89]
	v_mfma_f32_16x16x32_f16 v[82:85], v[210:213], v[186:189], v[82:85]
	v_mfma_f32_16x16x32_f16 v[70:73], v[202:205], v[194:197], v[70:73]
	v_mfma_f32_16x16x32_f16 v[66:69], v[210:213], v[194:197], v[66:69]
	s_mov_b32 m0, s49
	v_lshl_add_u64 v[142:143], v[216:217], 0, s[22:23]
	s_barrier
	ds_read_b128 v[166:169], v146 offset:49152
	ds_read_b128 v[170:173], v146 offset:50176
	ds_read_b128 v[174:177], v146 offset:51200
	ds_read_b128 v[178:181], v146 offset:52224
	ds_read_b128 v[182:185], v146 offset:53248
	ds_read_b128 v[186:189], v146 offset:54272
	ds_read_b128 v[190:193], v146 offset:55296
	ds_read_b128 v[194:197], v146 offset:56320
	global_load_lds_dwordx4 v[142:143], off
	v_lshl_add_u64 v[142:143], v[218:219], 0, s[22:23]
	s_mov_b32 m0, s50
	s_nop 0
	global_load_lds_dwordx4 v[142:143], off
	s_barrier
	s_waitcnt lgkmcnt(0)
	v_mfma_f32_16x16x32_f16 v[62:65], v[150:153], v[166:169], v[62:65]
	v_mfma_f32_16x16x32_f16 v[58:61], v[158:161], v[166:169], v[58:61]
	v_mfma_f32_16x16x32_f16 v[46:49], v[150:153], v[174:177], v[46:49]
	v_mfma_f32_16x16x32_f16 v[42:45], v[158:161], v[174:177], v[42:45]
	v_mfma_f32_16x16x32_f16 v[30:33], v[150:153], v[182:185], v[30:33]
	v_mfma_f32_16x16x32_f16 v[26:29], v[158:161], v[182:185], v[26:29]
	v_mfma_f32_16x16x32_f16 v[14:17], v[150:153], v[190:193], v[14:17]
	v_mfma_f32_16x16x32_f16 v[10:13], v[158:161], v[190:193], v[10:13]
	v_mfma_f32_16x16x32_f16 v[62:65], v[154:157], v[170:173], v[62:65]
	v_mfma_f32_16x16x32_f16 v[58:61], v[162:165], v[170:173], v[58:61]
	v_mfma_f32_16x16x32_f16 v[46:49], v[154:157], v[178:181], v[46:49]
	v_mfma_f32_16x16x32_f16 v[42:45], v[162:165], v[178:181], v[42:45]
	v_mfma_f32_16x16x32_f16 v[30:33], v[154:157], v[186:189], v[30:33]
	v_mfma_f32_16x16x32_f16 v[26:29], v[162:165], v[186:189], v[26:29]
	v_mfma_f32_16x16x32_f16 v[14:17], v[154:157], v[194:197], v[14:17]
	v_mfma_f32_16x16x32_f16 v[10:13], v[162:165], v[194:197], v[10:13]
	s_barrier
	s_add_i32 s28, s28, s40
	v_lshl_add_u64 v[142:143], v[220:221], 0, s[22:23]
	s_mov_b32 m0, s28
	s_nop 0
	global_load_lds_dwordx4 v[142:143], off
	v_lshl_add_u64 v[142:143], v[222:223], 0, s[22:23]
	s_add_i32 m0, s28, 0x2000
	s_nop 0
	global_load_lds_dwordx4 v[142:143], off
	s_waitcnt vmcnt(6)
	s_barrier
	v_mfma_f32_16x16x32_f16 v[54:57], v[198:201], v[166:169], v[54:57]
	v_mfma_f32_16x16x32_f16 v[50:53], v[206:209], v[166:169], v[50:53]
	v_mfma_f32_16x16x32_f16 v[38:41], v[198:201], v[174:177], v[38:41]
	v_mfma_f32_16x16x32_f16 v[34:37], v[206:209], v[174:177], v[34:37]
	v_mfma_f32_16x16x32_f16 v[22:25], v[198:201], v[182:185], v[22:25]
	v_mfma_f32_16x16x32_f16 v[18:21], v[206:209], v[182:185], v[18:21]
	v_mfma_f32_16x16x32_f16 v[6:9], v[198:201], v[190:193], v[6:9]
	v_mfma_f32_16x16x32_f16 v[2:5], v[206:209], v[190:193], v[2:5]
	v_mfma_f32_16x16x32_f16 v[54:57], v[202:205], v[170:173], v[54:57]
	v_mfma_f32_16x16x32_f16 v[50:53], v[210:213], v[170:173], v[50:53]
	v_mfma_f32_16x16x32_f16 v[38:41], v[202:205], v[178:181], v[38:41]
	v_mfma_f32_16x16x32_f16 v[34:37], v[210:213], v[178:181], v[34:37]
	v_mfma_f32_16x16x32_f16 v[22:25], v[202:205], v[186:189], v[22:25]
	v_mfma_f32_16x16x32_f16 v[18:21], v[210:213], v[186:189], v[18:21]
	v_mfma_f32_16x16x32_f16 v[6:9], v[202:205], v[194:197], v[6:9]
	v_mfma_f32_16x16x32_f16 v[2:5], v[210:213], v[194:197], v[2:5]
	s_add_u32 s63, s63, 0x100
	s_addc_u32 s64, s64, 0
	s_add_u32 s26, s26, 0x100
	s_addc_u32 s27, s27, 0
	s_cmp_ge_i32 s65, s51
	s_mov_b32 s28, s65
	s_barrier
	s_cbranch_scc0 .LBB2_21
	s_branch .LBB2_8

.LBB3_23:
	ds_read_b128 v[128:131], v169
	ds_read_b128 v[132:135], v169 offset:1024
	ds_read_b128 v[136:139], v169 offset:2048
	ds_read_b128 v[140:143], v169 offset:3072
	s_add_i32 s71, s34, 2
	s_add_u32 s36, s30, 0x80
	s_addc_u32 s35, s31, 0
	s_cmp_eq_u32 s62, s34
	s_cselect_b32 s34, s28, s36
	s_cselect_b32 s35, s29, s35
	s_cselect_b32 s37, s5, s70
	s_cselect_b32 s36, s4, s69
	v_lshl_add_u64 v[200:201], s[30:31], 0, v[150:151]
	s_add_i32 m0, s51, 0xc000
	ds_read_b128 v[154:157], v170
	ds_read_b128 v[172:175], v170 offset:1024
	ds_read_b128 v[176:179], v170 offset:2048
	ds_read_b128 v[180:183], v170 offset:3072
	ds_read_b128 v[184:187], v170 offset:4096
	ds_read_b128 v[188:191], v170 offset:5120
	ds_read_b128 v[192:195], v170 offset:6144
	ds_read_b128 v[196:199], v170 offset:7168
	global_load_lds_dwordx4 v[200:201], off
	v_lshl_add_u64 v[200:201], s[30:31], 0, v[148:149]
	s_add_i32 m0, s51, 0xe000
	s_nop 0
	global_load_lds_dwordx4 v[200:201], off
	s_waitcnt lgkmcnt(8)
	s_barrier
	s_waitcnt lgkmcnt(0)
	v_mfma_f32_16x16x32_f16 v[116:119], v[128:131], v[154:157], v[116:119]
	v_mfma_f32_16x16x32_f16 v[124:127], v[136:139], v[154:157], v[124:127]
	v_mfma_f32_16x16x32_f16 v[108:111], v[128:131], v[176:179], v[108:111]
	v_mfma_f32_16x16x32_f16 v[104:107], v[136:139], v[176:179], v[104:107]
	v_mfma_f32_16x16x32_f16 v[92:95], v[128:131], v[184:187], v[92:95]
	v_mfma_f32_16x16x32_f16 v[88:91], v[136:139], v[184:187], v[88:91]
	v_mfma_f32_16x16x32_f16 v[76:79], v[128:131], v[192:195], v[76:79]
	v_mfma_f32_16x16x32_f16 v[72:75], v[136:139], v[192:195], v[72:75]
	v_mfma_f32_16x16x32_f16 v[116:119], v[132:135], v[172:175], v[116:119]
	v_mfma_f32_16x16x32_f16 v[124:127], v[140:143], v[172:175], v[124:127]
	v_mfma_f32_16x16x32_f16 v[108:111], v[132:135], v[180:183], v[108:111]
	v_mfma_f32_16x16x32_f16 v[104:107], v[140:143], v[180:183], v[104:107]
	v_mfma_f32_16x16x32_f16 v[92:95], v[132:135], v[188:191], v[92:95]
	v_mfma_f32_16x16x32_f16 v[88:91], v[140:143], v[188:191], v[88:91]
	v_mfma_f32_16x16x32_f16 v[76:79], v[132:135], v[196:199], v[76:79]
	v_mfma_f32_16x16x32_f16 v[72:75], v[140:143], v[196:199], v[72:75]
	s_barrier
	s_add_i32 s72, s63, s40
	v_lshl_add_u64 v[216:217], s[36:37], 0, v[144:145]
	s_mov_b32 m0, s72
	ds_read_b128 v[200:203], v171
	ds_read_b128 v[204:207], v171 offset:1024
	ds_read_b128 v[208:211], v171 offset:2048
	ds_read_b128 v[212:215], v171 offset:3072
	global_load_lds_dwordx4 v[216:217], off
	v_lshl_add_u64 v[218:219], s[36:37], 0, v[146:147]
	s_add_i32 m0, s72, 0x2000
	s_nop 0
	global_load_lds_dwordx4 v[218:219], off
	s_barrier
	s_waitcnt lgkmcnt(0)
	v_mfma_f32_16x16x32_f16 v[120:123], v[200:203], v[154:157], v[120:123]
	v_mfma_f32_16x16x32_f16 v[112:115], v[208:211], v[154:157], v[112:115]
	v_mfma_f32_16x16x32_f16 v[100:103], v[200:203], v[176:179], v[100:103]
	v_mfma_f32_16x16x32_f16 v[96:99], v[208:211], v[176:179], v[96:99]
	v_mfma_f32_16x16x32_f16 v[84:87], v[200:203], v[184:187], v[84:87]
	v_mfma_f32_16x16x32_f16 v[80:83], v[208:211], v[184:187], v[80:83]
	v_mfma_f32_16x16x32_f16 v[68:71], v[200:203], v[192:195], v[68:71]
	v_mfma_f32_16x16x32_f16 v[64:67], v[208:211], v[192:195], v[64:67]
	v_mfma_f32_16x16x32_f16 v[120:123], v[204:207], v[172:175], v[120:123]
	v_mfma_f32_16x16x32_f16 v[112:115], v[212:215], v[172:175], v[112:115]
	v_mfma_f32_16x16x32_f16 v[100:103], v[204:207], v[180:183], v[100:103]
	v_mfma_f32_16x16x32_f16 v[96:99], v[212:215], v[180:183], v[96:99]
	v_mfma_f32_16x16x32_f16 v[84:87], v[204:207], v[188:191], v[84:87]
	v_mfma_f32_16x16x32_f16 v[80:83], v[212:215], v[188:191], v[80:83]
	v_mfma_f32_16x16x32_f16 v[68:71], v[204:207], v[196:199], v[68:71]
	v_mfma_f32_16x16x32_f16 v[64:67], v[212:215], v[196:199], v[64:67]
	s_mov_b32 m0, s51
	v_lshl_add_u64 v[220:221], s[34:35], 0, v[144:145]
	s_barrier
	ds_read_b128 v[154:157], v170 offset:16384
	ds_read_b128 v[172:175], v170 offset:17408
	ds_read_b128 v[176:179], v170 offset:18432
	ds_read_b128 v[180:183], v170 offset:19456
	ds_read_b128 v[184:187], v170 offset:20480
	ds_read_b128 v[188:191], v170 offset:21504
	ds_read_b128 v[192:195], v170 offset:22528
	ds_read_b128 v[196:199], v170 offset:23552
	global_load_lds_dwordx4 v[220:221], off
	v_lshl_add_u64 v[222:223], s[34:35], 0, v[146:147]
	s_mov_b32 m0, s52
	s_nop 0
	global_load_lds_dwordx4 v[222:223], off
	s_barrier
	s_waitcnt lgkmcnt(0)
	v_mfma_f32_16x16x32_f16 v[60:63], v[128:131], v[154:157], v[60:63]
	v_mfma_f32_16x16x32_f16 v[56:59], v[136:139], v[154:157], v[56:59]
	v_mfma_f32_16x16x32_f16 v[44:47], v[128:131], v[176:179], v[44:47]
	v_mfma_f32_16x16x32_f16 v[40:43], v[136:139], v[176:179], v[40:43]
	v_mfma_f32_16x16x32_f16 v[28:31], v[128:131], v[184:187], v[28:31]
	v_mfma_f32_16x16x32_f16 v[24:27], v[136:139], v[184:187], v[24:27]
	v_mfma_f32_16x16x32_f16 v[12:15], v[128:131], v[192:195], v[12:15]
	v_mfma_f32_16x16x32_f16 v[8:11], v[136:139], v[192:195], v[8:11]
	v_mfma_f32_16x16x32_f16 v[60:63], v[132:135], v[172:175], v[60:63]
	v_mfma_f32_16x16x32_f16 v[56:59], v[140:143], v[172:175], v[56:59]
	v_mfma_f32_16x16x32_f16 v[44:47], v[132:135], v[180:183], v[44:47]
	v_mfma_f32_16x16x32_f16 v[40:43], v[140:143], v[180:183], v[40:43]
	v_mfma_f32_16x16x32_f16 v[28:31], v[132:135], v[188:191], v[28:31]
	v_mfma_f32_16x16x32_f16 v[24:27], v[140:143], v[188:191], v[24:27]
	v_mfma_f32_16x16x32_f16 v[12:15], v[132:135], v[196:199], v[12:15]
	v_mfma_f32_16x16x32_f16 v[8:11], v[140:143], v[196:199], v[8:11]
	s_barrier
	s_add_u32 s36, s36, s20
	s_addc_u32 s37, s37, s21
	s_add_i32 s72, s64, s40
	v_lshl_add_u64 v[224:225], s[36:37], 0, v[144:145]
	s_mov_b32 m0, s72
	v_lshl_add_u64 v[226:227], s[36:37], 0, v[146:147]
	global_load_lds_dwordx4 v[224:225], off
	s_add_i32 m0, s72, 0x2000
	s_nop 0
	global_load_lds_dwordx4 v[226:227], off
	s_waitcnt vmcnt(6)
	s_barrier
	v_mfma_f32_16x16x32_f16 v[52:55], v[200:203], v[154:157], v[52:55]
	v_mfma_f32_16x16x32_f16 v[48:51], v[208:211], v[154:157], v[48:51]
	v_mfma_f32_16x16x32_f16 v[36:39], v[200:203], v[176:179], v[36:39]
	v_mfma_f32_16x16x32_f16 v[32:35], v[208:211], v[176:179], v[32:35]
	v_mfma_f32_16x16x32_f16 v[20:23], v[200:203], v[184:187], v[20:23]
	v_mfma_f32_16x16x32_f16 v[16:19], v[208:211], v[184:187], v[16:19]
	v_mfma_f32_16x16x32_f16 v[4:7], v[200:203], v[192:195], v[4:7]
	v_mfma_f32_16x16x32_f16 v[0:3], v[208:211], v[192:195], v[0:3]
	v_mfma_f32_16x16x32_f16 v[52:55], v[204:207], v[172:175], v[52:55]
	v_mfma_f32_16x16x32_f16 v[48:51], v[212:215], v[172:175], v[48:51]
	v_mfma_f32_16x16x32_f16 v[36:39], v[204:207], v[180:183], v[36:39]
	v_mfma_f32_16x16x32_f16 v[32:35], v[212:215], v[180:183], v[32:35]
	v_mfma_f32_16x16x32_f16 v[20:23], v[204:207], v[188:191], v[20:23]
	v_mfma_f32_16x16x32_f16 v[16:19], v[212:215], v[188:191], v[16:19]
	v_mfma_f32_16x16x32_f16 v[4:7], v[204:207], v[196:199], v[4:7]
	v_mfma_f32_16x16x32_f16 v[0:3], v[212:215], v[196:199], v[0:3]
	s_add_i32 s36, 0, 0x18000
	v_add_u32_e32 v140, s36, v161
	s_barrier
	ds_read_b128 v[128:131], v140
	ds_read_b128 v[132:135], v140 offset:1024
	ds_read_b128 v[136:139], v140 offset:2048
	ds_read_b128 v[140:143], v140 offset:3072
	s_add_u32 s34, s34, s20
	s_addc_u32 s35, s35, s21
	s_mov_b32 m0, s53
	v_lshl_add_u64 v[200:201], s[34:35], 0, v[144:145]
	ds_read_b128 v[154:157], v170 offset:32768
	ds_read_b128 v[172:175], v170 offset:33792
	ds_read_b128 v[176:179], v170 offset:34816
	ds_read_b128 v[180:183], v170 offset:35840
	ds_read_b128 v[184:187], v170 offset:36864
	ds_read_b128 v[188:191], v170 offset:37888
	ds_read_b128 v[192:195], v170 offset:38912
	ds_read_b128 v[196:199], v170 offset:39936
	global_load_lds_dwordx4 v[200:201], off
	v_lshl_add_u64 v[200:201], s[34:35], 0, v[146:147]
	s_mov_b32 m0, s54
	s_nop 0
	global_load_lds_dwordx4 v[200:201], off
	s_waitcnt lgkmcnt(8)
	s_barrier
	s_waitcnt lgkmcnt(0)
	v_mfma_f32_16x16x32_f16 v[116:119], v[128:131], v[154:157], v[116:119]
	v_mfma_f32_16x16x32_f16 v[124:127], v[136:139], v[154:157], v[124:127]
	v_mfma_f32_16x16x32_f16 v[108:111], v[128:131], v[176:179], v[108:111]
	v_mfma_f32_16x16x32_f16 v[104:107], v[136:139], v[176:179], v[104:107]
	v_mfma_f32_16x16x32_f16 v[92:95], v[128:131], v[184:187], v[92:95]
	v_mfma_f32_16x16x32_f16 v[88:91], v[136:139], v[184:187], v[88:91]
	v_mfma_f32_16x16x32_f16 v[76:79], v[128:131], v[192:195], v[76:79]
	v_mfma_f32_16x16x32_f16 v[72:75], v[136:139], v[192:195], v[72:75]
	v_mfma_f32_16x16x32_f16 v[116:119], v[132:135], v[172:175], v[116:119]
	v_mfma_f32_16x16x32_f16 v[124:127], v[140:143], v[172:175], v[124:127]
	v_mfma_f32_16x16x32_f16 v[108:111], v[132:135], v[180:183], v[108:111]
	v_mfma_f32_16x16x32_f16 v[104:107], v[140:143], v[180:183], v[104:107]
	v_mfma_f32_16x16x32_f16 v[92:95], v[132:135], v[188:191], v[92:95]
	v_mfma_f32_16x16x32_f16 v[88:91], v[140:143], v[188:191], v[88:91]
	v_mfma_f32_16x16x32_f16 v[76:79], v[132:135], v[196:199], v[76:79]
	v_mfma_f32_16x16x32_f16 v[72:75], v[140:143], v[196:199], v[72:75]
	s_barrier
	s_add_i32 s34, 0, 0x1c000
	s_add_i32 s35, s36, s40
	v_add_u32_e32 v212, s34, v161
	v_lshl_add_u64 v[216:217], v[216:217], 0, s[24:25]
	s_mov_b32 m0, s35
	ds_read_b128 v[200:203], v212
	ds_read_b128 v[204:207], v212 offset:1024
	ds_read_b128 v[208:211], v212 offset:2048
	ds_read_b128 v[212:215], v212 offset:3072
	global_load_lds_dwordx4 v[216:217], off
	v_lshl_add_u64 v[216:217], v[218:219], 0, s[24:25]
	s_add_i32 m0, s35, 0x2000
	s_nop 0
	global_load_lds_dwordx4 v[216:217], off
	s_barrier
	s_waitcnt lgkmcnt(0)
	v_mfma_f32_16x16x32_f16 v[120:123], v[200:203], v[154:157], v[120:123]
	v_mfma_f32_16x16x32_f16 v[112:115], v[208:211], v[154:157], v[112:115]
	v_mfma_f32_16x16x32_f16 v[100:103], v[200:203], v[176:179], v[100:103]
	v_mfma_f32_16x16x32_f16 v[96:99], v[208:211], v[176:179], v[96:99]
	v_mfma_f32_16x16x32_f16 v[84:87], v[200:203], v[184:187], v[84:87]
	v_mfma_f32_16x16x32_f16 v[80:83], v[208:211], v[184:187], v[80:83]
	v_mfma_f32_16x16x32_f16 v[68:71], v[200:203], v[192:195], v[68:71]
	v_mfma_f32_16x16x32_f16 v[64:67], v[208:211], v[192:195], v[64:67]
	v_mfma_f32_16x16x32_f16 v[120:123], v[204:207], v[172:175], v[120:123]
	v_mfma_f32_16x16x32_f16 v[112:115], v[212:215], v[172:175], v[112:115]
	v_mfma_f32_16x16x32_f16 v[100:103], v[204:207], v[180:183], v[100:103]
	v_mfma_f32_16x16x32_f16 v[96:99], v[212:215], v[180:183], v[96:99]
	v_mfma_f32_16x16x32_f16 v[84:87], v[204:207], v[188:191], v[84:87]
	v_mfma_f32_16x16x32_f16 v[80:83], v[212:215], v[188:191], v[80:83]
	v_mfma_f32_16x16x32_f16 v[68:71], v[204:207], v[196:199], v[68:71]
	v_mfma_f32_16x16x32_f16 v[64:67], v[212:215], v[196:199], v[64:67]
	s_mov_b32 m0, s57
	v_lshl_add_u64 v[216:217], v[220:221], 0, s[24:25]
	s_barrier
	ds_read_b128 v[154:157], v170 offset:49152
	ds_read_b128 v[172:175], v170 offset:50176
	ds_read_b128 v[176:179], v170 offset:51200
	ds_read_b128 v[180:183], v170 offset:52224
	ds_read_b128 v[184:187], v170 offset:53248
	ds_read_b128 v[188:191], v170 offset:54272
	ds_read_b128 v[192:195], v170 offset:55296
	ds_read_b128 v[196:199], v170 offset:56320
	global_load_lds_dwordx4 v[216:217], off
	v_lshl_add_u64 v[216:217], v[222:223], 0, s[24:25]
	s_mov_b32 m0, s58
	s_nop 0
	global_load_lds_dwordx4 v[216:217], off
	s_barrier
	s_waitcnt lgkmcnt(0)
	v_mfma_f32_16x16x32_f16 v[60:63], v[128:131], v[154:157], v[60:63]
	v_mfma_f32_16x16x32_f16 v[56:59], v[136:139], v[154:157], v[56:59]
	v_mfma_f32_16x16x32_f16 v[44:47], v[128:131], v[176:179], v[44:47]
	v_mfma_f32_16x16x32_f16 v[40:43], v[136:139], v[176:179], v[40:43]
	v_mfma_f32_16x16x32_f16 v[28:31], v[128:131], v[184:187], v[28:31]
	v_mfma_f32_16x16x32_f16 v[24:27], v[136:139], v[184:187], v[24:27]
	v_mfma_f32_16x16x32_f16 v[12:15], v[128:131], v[192:195], v[12:15]
	v_mfma_f32_16x16x32_f16 v[8:11], v[136:139], v[192:195], v[8:11]
	v_mfma_f32_16x16x32_f16 v[60:63], v[132:135], v[172:175], v[60:63]
	v_mfma_f32_16x16x32_f16 v[56:59], v[140:143], v[172:175], v[56:59]
	v_mfma_f32_16x16x32_f16 v[44:47], v[132:135], v[180:183], v[44:47]
	v_mfma_f32_16x16x32_f16 v[40:43], v[140:143], v[180:183], v[40:43]
	v_mfma_f32_16x16x32_f16 v[28:31], v[132:135], v[188:191], v[28:31]
	v_mfma_f32_16x16x32_f16 v[24:27], v[140:143], v[188:191], v[24:27]
	v_mfma_f32_16x16x32_f16 v[12:15], v[132:135], v[196:199], v[12:15]
	v_mfma_f32_16x16x32_f16 v[8:11], v[140:143], v[196:199], v[8:11]
	s_barrier
	s_add_i32 s34, s34, s40
	v_lshl_add_u64 v[128:129], v[224:225], 0, s[24:25]
	s_mov_b32 m0, s34
	s_nop 0
	global_load_lds_dwordx4 v[128:129], off
	v_lshl_add_u64 v[128:129], v[226:227], 0, s[24:25]
	s_add_i32 m0, s34, 0x2000
	s_nop 0
	global_load_lds_dwordx4 v[128:129], off
	s_waitcnt vmcnt(6)
	s_barrier
	v_mfma_f32_16x16x32_f16 v[52:55], v[200:203], v[154:157], v[52:55]
	v_mfma_f32_16x16x32_f16 v[48:51], v[208:211], v[154:157], v[48:51]
	v_mfma_f32_16x16x32_f16 v[36:39], v[200:203], v[176:179], v[36:39]
	v_mfma_f32_16x16x32_f16 v[32:35], v[208:211], v[176:179], v[32:35]
	v_mfma_f32_16x16x32_f16 v[20:23], v[200:203], v[184:187], v[20:23]
	v_mfma_f32_16x16x32_f16 v[16:19], v[208:211], v[184:187], v[16:19]
	v_mfma_f32_16x16x32_f16 v[4:7], v[200:203], v[192:195], v[4:7]
	v_mfma_f32_16x16x32_f16 v[0:3], v[208:211], v[192:195], v[0:3]
	v_mfma_f32_16x16x32_f16 v[52:55], v[204:207], v[172:175], v[52:55]
	v_mfma_f32_16x16x32_f16 v[48:51], v[212:215], v[172:175], v[48:51]
	v_mfma_f32_16x16x32_f16 v[36:39], v[204:207], v[180:183], v[36:39]
	v_mfma_f32_16x16x32_f16 v[32:35], v[212:215], v[180:183], v[32:35]
	v_mfma_f32_16x16x32_f16 v[20:23], v[204:207], v[188:191], v[20:23]
	v_mfma_f32_16x16x32_f16 v[16:19], v[212:215], v[188:191], v[16:19]
	v_mfma_f32_16x16x32_f16 v[4:7], v[204:207], v[196:199], v[4:7]
	v_mfma_f32_16x16x32_f16 v[0:3], v[212:215], v[196:199], v[0:3]
	s_add_u32 s69, s69, 0x100
	s_addc_u32 s70, s70, 0
	s_add_u32 s30, s30, 0x100
	s_addc_u32 s31, s31, 0
	s_cmp_ge_i32 s71, s39
	s_mov_b32 s34, s71
	s_barrier
	s_cbranch_scc0 .LBB3_23
	s_branch .LBB3_10
